# phase 11 V transpose: bid rotated so that an XCD owns 32 consecutive 64-token units (the two units of an output line share an XCD)
# baseline (speedup 1.0000x reference)
; __device__ __forceinline__ float bf2f(bfr h) { return __uint_as_float(((unsigned)h) << 16); }
; __device__ __forceinline__ unsigned char f2fp8(float f) { return (unsigned char)(__builtin_amdgcn_cvt_pk_fp8_f32(f, f, 0, false) & 0xff); }
; __device__ __forceinline__ void phase_qkprep_s5a(const Params& P, float* sm, int bid, int nb) {
;     ...
;     {
;         unsigned char* VT = (unsigned char*)(P.ws + WS_VT);
;         unsigned char* tile = (unsigned char*)sm;
;         for (int u = bid; u < NT / 64; u += nb) {
;             __syncthreads();
;             for (int e = threadIdx.x; e < 64 * 128; e += NTHR) {
;                 const int r = e >> 7, c = e & 127;
;                 const int pos = ((r >> 2) & 1) * 32 + (r >> 5) * 16 + ((r >> 3) & 3) * 4 + (r & 3);
;                 tile[c * 68 + pos] = f2fp8(bf2f(QK[(size_t)(u * 64 + r) * 1280 + 640 + c]));
;             }
;             __syncthreads();
;             for (int e = threadIdx.x; e < 128 * 16; e += NTHR) { const int c = e >> 4, w = e & 15; *(unsigned*)&VT[(size_t)c * NT + u * 64 + w * 4] = *(const unsigned*)&tile[c * 68 + w * 4]; }
;         }
.LBB0_1816:
	s_or_b64 exec, exec, s[10:11]
	v_readlane_b32 s96, v253, 10
	s_cmpk_lg_u32 s96, 0x100
	s_mov_b32 s96, s44
	s_cbranch_scc1 .Lvt_xcd
	s_and_b32 s96, s44, 7
	s_lshl_b32 s96, s96, 5
	s_lshr_b32 s97, s44, 3
	s_or_b32 s96, s96, s97
.Lvt_xcd:
	s_cmpk_gt_i32 s96, 0x103
	s_cbranch_scc1 .LBB0_1823
	v_and_b32_e32 v2, 0x7f, v0
	s_movk_i32 s6, 0x44
	v_lshrrev_b32_e32 v12, 4, v0
	v_and_b32_e32 v6, 15, v0
	v_mad_u32_u24 v9, v2, s6, 0
	v_lshlrev_b32_e32 v2, 1, v2
	v_mov_b32_e32 v3, 0
	v_readlane_b32 s4, v253, 10
	v_mul_u32_u24_e32 v4, 0x4100, v12
	v_lshlrev_b32_e32 v6, 2, v6
	v_lshl_add_u64 v[2:3], s[42:43], 0, v[2:3]
	s_mov_b64 s[0:1], 0x7078000
	v_readlane_b32 s5, v253, 11
	v_mul_hi_u32_u24_e32 v5, 0x4100, v12
	v_or_b32_e32 v4, v4, v6
	v_lshrrev_b32_e32 v8, 7, v0
	v_lshl_add_u64 v[2:3], v[2:3], 0, s[0:1]
	s_lshl_b32 s0, s96, 6
	s_lshl_b32 s3, s4, 6
	v_lshl_add_u64 v[4:5], s[42:43], 0, v[4:5]
	s_mov_b64 s[4:5], 0x3c152400
	v_mad_u32_u24 v6, v12, s6, v6
	v_or_b32_e32 v10, 0xfffffe00, v0
	v_lshrrev_b32_e32 v11, 8, v0
	v_or_b32_e32 v13, s0, v8
	v_lshl_add_u64 v[4:5], v[4:5], 0, s[4:5]
	v_add3_u32 v14, v6, 0, 16
	s_movk_i32 s8, 0xa00
	s_movk_i32 s9, 0x1dff
	s_mov_b64 s[4:5], 0x82000
	s_movk_i32 s10, 0x5ff
	s_mov_b32 s11, s96
